# waitcnt placement: attention loop top drops the first of two back-to-back s_waitcnt vmcnt(0) and the now-dead s_cmp before the barrier (both instantiations); on top of v65
# speedup vs baseline: 1.0009x; 1.0009x over previous
.Lprio_skip_a1:
.LBB0_805:
	s_add_i32 s56, s12, -1

	s_and_b32 s87, s56, 1
	s_mul_i32 s56, s87, 0x6000
	s_add_i32 s56, s56, 0
	s_add_i32 s56, s56, 0x8000
	v_add_u32_e32 v175, s56, v161
	v_add_u32_e32 v200, s56, v169
	v_add_u32_e32 v201, s56, v170

	s_waitcnt vmcnt(0) lgkmcnt(0)
	s_barrier



.Lprio_skip_a2:
.LBB0_946:
	s_add_i32 s44, s12, -1

	s_and_b32 s48, s44, 1
	s_mul_i32 s44, s48, 0x6000
	s_add_i32 s44, s44, 0
	s_add_i32 s44, s44, 0x8000
	v_add_u32_e32 v177, s44, v171
	v_add_u32_e32 v206, s44, v172
	v_add_u32_e32 v207, s44, v173

	s_waitcnt vmcnt(0) lgkmcnt(0)
	s_barrier


